# speedup vs baseline: 1.0264x; 1.0022x over previous
.LBB1_6:
	s_waitcnt lgkmcnt(14)
	v_mfma_f32_32x32x16_f16 v[34:49], v[162:165], v[122:125], v[34:49]
	v_exp_f32_e32 v98, v98
	v_exp_f32_e32 v99, v99
	v_exp_f32_e32 v100, v100
	v_exp_f32_e32 v101, v101
	s_sub_i32 s43, s38, s27
	s_add_i32 s43, s43, 34
	s_add_i32 s44, s18, -1
	s_cmp_ge_i32 s44, s28
	s_cselect_b32 s45, s28, 0
	s_sub_i32 s44, s44, s45
	s_and_b64 s[48:49], s[6:7], exec
	s_cselect_b32 s43, s44, s43
	v_mad_i64_i32 v[252:253], s[50:51], s43, v244, v[222:223]
	s_add_i32 s44, s38, 1
	s_cmp_ge_i32 s44, s29
	s_cselect_b32 s44, s29, 0
	s_sub_i32 s44, 0, s44
	s_and_b64 s[48:49], s[6:7], exec
	s_cselect_b32 s44, s44, s28
	s_add_i32 s44, s44, s18
	s_add_i32 s44, s44, -3
	v_mad_i64_i32 v[254:255], s[50:51], s44, v244, v[224:225]
	s_waitcnt lgkmcnt(12)
	v_mfma_f32_32x32x16_f16 v[18:33], v[162:165], v[118:121], v[18:33]
	v_exp_f32_e32 v102, v102
	v_exp_f32_e32 v103, v103
	v_exp_f32_e32 v104, v104
	v_exp_f32_e32 v105, v105
	v_add_u32_e32 v74, s36, v234
	ds_read_b128 v[62:65], v74
	ds_read_b128 v[138:141], v74 offset:4096
	s_waitcnt lgkmcnt(12)
	v_mfma_f32_32x32x16_f16 v[34:49], v[166:169], v[114:117], v[34:49]
	v_exp_f32_e32 v106, v106
	v_exp_f32_e32 v107, v107
	v_exp_f32_e32 v108, v108
	v_exp_f32_e32 v109, v109
	v_add_u32_e32 v74, s36, v235
	ds_read_b128 v[178:181], v74
	ds_read_b128 v[126:129], v74 offset:4096
	s_waitcnt lgkmcnt(12)
	v_mfma_f32_32x32x16_f16 v[18:33], v[166:169], v[70:73], v[18:33]
	v_exp_f32_e32 v110, v110
	v_exp_f32_e32 v111, v111
	v_exp_f32_e32 v112, v112
	v_exp_f32_e32 v113, v113
	v_add_u32_e32 v70, s36, v236
	ds_read_b128 v[130:133], v70
	ds_read_b128 v[118:121], v70 offset:4096
	s_waitcnt lgkmcnt(12)
	v_mfma_f32_32x32x16_f16 v[34:49], v[170:173], v[66:69], v[34:49]
	v_exp_f32_e32 v82, v82
	v_exp_f32_e32 v83, v83
	v_exp_f32_e32 v84, v84
	v_exp_f32_e32 v85, v85
	v_add_u32_e32 v66, s36, v237
	ds_read_b128 v[122:125], v66
	ds_read_b128 v[114:117], v66 offset:4096
	s_waitcnt lgkmcnt(12)
	v_mfma_f32_32x32x16_f16 v[18:33], v[170:173], v[50:53], v[18:33]
	v_exp_f32_e32 v86, v86
	v_exp_f32_e32 v87, v87
	v_exp_f32_e32 v88, v88
	v_exp_f32_e32 v89, v89
	s_waitcnt lgkmcnt(10)
	v_mfma_f32_32x32x16_f16 v[34:49], v[174:177], v[54:57], v[34:49]
	v_exp_f32_e32 v90, v90
	v_exp_f32_e32 v91, v91
	v_exp_f32_e32 v92, v92
	v_exp_f32_e32 v93, v93
	s_waitcnt lgkmcnt(8)
	v_mfma_f32_32x32x16_f16 v[18:33], v[174:177], v[58:61], v[18:33]
	v_exp_f32_e32 v94, v94
	v_exp_f32_e32 v95, v95
	v_exp_f32_e32 v96, v96
	v_exp_f32_e32 v97, v97
	v_cndmask_b32_e64 v50, 0, 1, s[12:13]
	v_cmp_ne_u32_e64 s[4:5], 1, v50
	s_add_i32 s16, s35, s30
	s_mov_b32 m0, s16
	s_nop 0
	global_load_lds_dwordx4 v[252:253], off
	s_addk_i32 s16, 0x1000
	v_lshl_add_u64 v[252:253], v[252:253], 0, s[10:11]
	s_mov_b32 m0, s16
	s_nop 0
	global_load_lds_dwordx4 v[252:253], off
	s_add_i32 s16, s36, s31
	s_mov_b32 m0, s16
	s_nop 0
	global_load_lds_dwordx4 v[254:255], off
	v_lshl_add_u64 v[254:255], v[254:255], 0, s[10:11]
	s_addk_i32 s16, 0x1000
	s_mov_b32 m0, s16
	s_nop 0
	global_load_lds_dwordx4 v[254:255], off
	s_waitcnt vmcnt(4) lgkmcnt(0)
	s_barrier
	s_andn2_b64 vcc, exec, s[8:9]
	s_cbranch_vccnz .LBB1_12
	v_add_u32_e32 v66, s24, v233
	ds_read_b128 v[50:53], v66 offset:96
	ds_read_b128 v[54:57], v66 offset:64
	ds_read_b128 v[58:61], v66 offset:32
	ds_read_b128 v[66:69], v66
	s_waitcnt lgkmcnt(3)
	v_pk_mul_f32 v[46:47], v[46:47], v[50:51]
	s_waitcnt lgkmcnt(2)
	v_pk_mul_f32 v[42:43], v[42:43], v[54:55]
	s_waitcnt lgkmcnt(1)
	v_pk_mul_f32 v[38:39], v[38:39], v[58:59]
	v_pk_mul_f32 v[48:49], v[48:49], v[52:53]
	v_pk_mul_f32 v[44:45], v[44:45], v[56:57]
	v_pk_mul_f32 v[40:41], v[40:41], v[60:61]
	s_waitcnt lgkmcnt(0)
	v_pk_mul_f32 v[36:37], v[36:37], v[68:69]
	v_pk_mul_f32 v[34:35], v[34:35], v[66:67]
	v_pk_mul_f32 v[30:31], v[30:31], v[50:51]
	v_pk_mul_f32 v[26:27], v[26:27], v[54:55]
	v_pk_mul_f32 v[22:23], v[22:23], v[58:59]
	v_pk_mul_f32 v[32:33], v[32:33], v[52:53]
	v_pk_mul_f32 v[28:29], v[28:29], v[56:57]
	v_pk_mul_f32 v[24:25], v[24:25], v[60:61]
	v_pk_mul_f32 v[20:21], v[20:21], v[68:69]
	v_pk_mul_f32 v[18:19], v[18:19], v[66:67]

.LBB1_13:
	s_add_i32 s16, s36, 0x2000
	s_cmpk_lg_i32 s36, 0x4000
	s_cselect_b32 s35, s16, 0
	s_waitcnt lgkmcnt(14)
	v_mfma_f32_32x32x16_f16 v[34:49], v[162:165], v[134:137], v[34:49]
	v_exp_f32_e32 v66, v66
	v_exp_f32_e32 v67, v67
	v_exp_f32_e32 v68, v68
	v_exp_f32_e32 v69, v69
	s_sub_i32 s43, s38, s27
	s_add_i32 s45, s43, 33
	s_add_i32 s43, s43, 35
	s_cmp_ge_i32 s18, s28
	s_cselect_b32 s44, s28, 0
	s_sub_i32 s44, s18, s44
	s_and_b64 s[48:49], s[6:7], exec
	s_cselect_b32 s43, s44, s43
	v_mad_i64_i32 v[252:253], s[50:51], s43, v244, v[222:223]
	s_add_i32 s44, s18, -2
	s_cmp_ge_i32 s44, s28
	s_cselect_b32 s46, s28, 0
	s_sub_i32 s44, s44, s46
	s_and_b64 s[48:49], s[6:7], exec
	s_cselect_b32 s44, s44, s45
	v_mad_i64_i32 v[254:255], s[50:51], s44, v244, v[224:225]
	s_waitcnt lgkmcnt(12)
	v_mfma_f32_32x32x16_f16 v[18:33], v[162:165], v[142:145], v[18:33]
	v_exp_f32_e32 v70, v70
	v_exp_f32_e32 v71, v71
	v_exp_f32_e32 v72, v72
	v_exp_f32_e32 v73, v73
	v_add_u32_e32 v94, s35, v234
	ds_read_b128 v[206:209], v94
	ds_read_b128 v[202:205], v94 offset:4096
	s_waitcnt lgkmcnt(12)
	v_mfma_f32_32x32x16_f16 v[34:49], v[166:169], v[138:141], v[34:49]
	v_exp_f32_e32 v74, v74
	v_exp_f32_e32 v75, v75
	v_exp_f32_e32 v76, v76
	v_exp_f32_e32 v77, v77
	v_add_u32_e32 v94, s35, v235
	ds_read_b128 v[198:201], v94
	ds_read_b128 v[194:197], v94 offset:4096
	s_waitcnt lgkmcnt(12)
	v_mfma_f32_32x32x16_f16 v[18:33], v[166:169], v[102:105], v[18:33]
	v_exp_f32_e32 v78, v78
	v_exp_f32_e32 v79, v79
	v_exp_f32_e32 v80, v80
	v_exp_f32_e32 v81, v81
	v_add_u32_e32 v94, s35, v236
	ds_read_b128 v[190:193], v94
	ds_read_b128 v[186:189], v94 offset:4096
	s_waitcnt lgkmcnt(12)
	v_mfma_f32_32x32x16_f16 v[34:49], v[170:173], v[98:101], v[34:49]
	v_exp_f32_e32 v50, v50
	v_exp_f32_e32 v51, v51
	v_exp_f32_e32 v52, v52
	v_exp_f32_e32 v53, v53
	v_add_u32_e32 v94, s35, v237
	ds_read_b128 v[182:185], v94
	ds_read_b128 v[178:181], v94 offset:4096
	s_waitcnt lgkmcnt(12)
	v_mfma_f32_32x32x16_f16 v[18:33], v[170:173], v[82:85], v[18:33]
	v_exp_f32_e32 v54, v54
	v_exp_f32_e32 v55, v55
	v_exp_f32_e32 v56, v56
	v_exp_f32_e32 v57, v57
	s_waitcnt lgkmcnt(10)
	v_mfma_f32_32x32x16_f16 v[34:49], v[174:177], v[86:89], v[34:49]
	v_exp_f32_e32 v58, v58
	v_exp_f32_e32 v59, v59
	v_exp_f32_e32 v60, v60
	v_exp_f32_e32 v61, v61
	s_waitcnt lgkmcnt(8)
	v_mfma_f32_32x32x16_f16 v[18:33], v[174:177], v[90:93], v[18:33]
	v_exp_f32_e32 v62, v62
	v_exp_f32_e32 v63, v63
	v_exp_f32_e32 v64, v64
	v_exp_f32_e32 v65, v65
	s_add_i32 s16, s36, s30
	s_mov_b32 m0, s16
	s_nop 0
	global_load_lds_dwordx4 v[252:253], off
	v_lshl_add_u64 v[252:253], v[252:253], 0, s[10:11]
	s_addk_i32 s16, 0x1000
	s_mov_b32 m0, s16
	s_nop 0
	global_load_lds_dwordx4 v[252:253], off
	s_add_i32 s4, s35, s31
	s_mov_b32 m0, s4
	s_nop 0
	global_load_lds_dwordx4 v[254:255], off
	v_lshl_add_u64 v[254:255], v[254:255], 0, s[10:11]
	s_addk_i32 s4, 0x1000
	s_mov_b32 m0, s4
	s_nop 0
	global_load_lds_dwordx4 v[254:255], off
	s_waitcnt vmcnt(4) lgkmcnt(0)
	s_barrier
	s_andn2_b64 vcc, exec, s[8:9]
	s_cbranch_vccnz .LBB1_23
	v_add_u32_e32 v94, s24, v233
	ds_read_b128 v[82:85], v94 offset:96
	ds_read_b128 v[86:89], v94 offset:64
	ds_read_b128 v[90:93], v94
	ds_read_b128 v[94:97], v94 offset:32
	s_waitcnt lgkmcnt(3)
	v_pk_mul_f32 v[48:49], v[48:49], v[84:85]
	v_pk_mul_f32 v[46:47], v[46:47], v[82:83]
	s_waitcnt lgkmcnt(2)
	v_pk_mul_f32 v[44:45], v[44:45], v[88:89]
	v_pk_mul_f32 v[42:43], v[42:43], v[86:87]
	s_waitcnt lgkmcnt(0)
	v_pk_mul_f32 v[40:41], v[40:41], v[96:97]
	v_pk_mul_f32 v[38:39], v[38:39], v[94:95]
	v_pk_mul_f32 v[36:37], v[36:37], v[92:93]
	v_pk_mul_f32 v[34:35], v[34:35], v[90:91]
	v_pk_mul_f32 v[32:33], v[32:33], v[84:85]
	v_pk_mul_f32 v[30:31], v[30:31], v[82:83]
	v_pk_mul_f32 v[28:29], v[28:29], v[88:89]
	v_pk_mul_f32 v[26:27], v[26:27], v[86:87]
	v_pk_mul_f32 v[24:25], v[24:25], v[96:97]
	v_pk_mul_f32 v[22:23], v[22:23], v[94:95]
	v_pk_mul_f32 v[20:21], v[20:21], v[92:93]
	v_pk_mul_f32 v[18:19], v[18:19], v[90:91]

	.amdhsa_kernel _Z10attn64_fwdPKDF16_S0_S0_PDF16_
		.amdhsa_group_segment_fixed_size 0
		.amdhsa_private_segment_fixed_size 0
		.amdhsa_kernarg_size 32
		.amdhsa_user_sgpr_count 2
		.amdhsa_user_sgpr_dispatch_ptr 0
		.amdhsa_user_sgpr_queue_ptr 0
		.amdhsa_user_sgpr_kernarg_segment_ptr 1
		.amdhsa_user_sgpr_dispatch_id 0
		.amdhsa_user_sgpr_kernarg_preload_length 0
		.amdhsa_user_sgpr_kernarg_preload_offset 0
		.amdhsa_user_sgpr_private_segment_size 0
		.amdhsa_uses_dynamic_stack 0
		.amdhsa_enable_private_segment 0
		.amdhsa_system_sgpr_workgroup_id_x 1
		.amdhsa_system_sgpr_workgroup_id_y 0
		.amdhsa_system_sgpr_workgroup_id_z 0
		.amdhsa_system_sgpr_workgroup_info 0
		.amdhsa_system_vgpr_workitem_id 0
		.amdhsa_next_free_vgpr 256
		.amdhsa_next_free_sgpr 52
		.amdhsa_accum_offset 256
		.amdhsa_reserve_vcc 1
		.amdhsa_float_round_mode_32 0
		.amdhsa_float_round_mode_16_64 0
		.amdhsa_float_denorm_mode_32 3
		.amdhsa_float_denorm_mode_16_64 3
		.amdhsa_dx10_clamp 1
		.amdhsa_ieee_mode 1
		.amdhsa_fp16_overflow 0
		.amdhsa_tg_split 0
		.amdhsa_exception_fp_ieee_invalid_op 0
		.amdhsa_exception_fp_denorm_src 0
		.amdhsa_exception_fp_ieee_div_zero 0
		.amdhsa_exception_fp_ieee_overflow 0
		.amdhsa_exception_fp_ieee_underflow 0
		.amdhsa_exception_fp_ieee_inexact 0
		.amdhsa_exception_int_div_zero 0
	.end_amdhsa_kernel

amdhsa.kernels:
  - .agpr_count:     0
    .args:
      - .actual_access:  read_only
        .address_space:  global
        .offset:         0
        .size:           8
        .value_kind:     global_buffer
      - .actual_access:  read_only
        .address_space:  global
        .offset:         8
        .size:           8
        .value_kind:     global_buffer
      - .actual_access:  read_only
        .address_space:  global
        .offset:         16
        .size:           8
        .value_kind:     global_buffer
      - .actual_access:  read_only
        .address_space:  global
        .offset:         24
        .size:           8
        .value_kind:     global_buffer
      - .actual_access:  read_only
        .address_space:  global
        .offset:         32
        .size:           8
        .value_kind:     global_buffer
      - .address_space:  global
        .offset:         40
        .size:           8
        .value_kind:     global_buffer
      - .address_space:  global
        .offset:         48
        .size:           8
        .value_kind:     global_buffer
      - .address_space:  global
        .offset:         56
        .size:           8
        .value_kind:     global_buffer
      - .address_space:  global
        .offset:         64
        .size:           8
        .value_kind:     global_buffer
    .group_segment_fixed_size: 0
    .kernarg_segment_align: 8
    .kernarg_segment_size: 72
    .language:       OpenCL C
    .language_version:
      - 2
      - 0
    .max_flat_workgroup_size: 256
    .name:           _Z11prep_kernelPKfS0_S0_S0_S0_PDF16_S1_S1_P15HIP_vector_typeIfLj2EE
    .private_segment_fixed_size: 0
    .sgpr_count:     32
    .sgpr_spill_count: 0
    .symbol:         _Z11prep_kernelPKfS0_S0_S0_S0_PDF16_S1_S1_P15HIP_vector_typeIfLj2EE.kd
    .uniform_work_group_size: 1
    .uses_dynamic_stack: false
    .vgpr_count:     20
    .vgpr_spill_count: 0
    .wavefront_size: 64
  - .agpr_count:     0
    .args:
      - .address_space:  global
        .offset:         0
        .size:           8
        .value_kind:     global_buffer
      - .address_space:  global
        .offset:         8
        .size:           8
        .value_kind:     global_buffer
      - .address_space:  global
        .offset:         16
        .size:           8
        .value_kind:     global_buffer
      - .address_space:  global
        .offset:         24
        .size:           8
        .value_kind:     global_buffer
    .group_segment_fixed_size: 0
    .kernarg_segment_align: 8
    .kernarg_segment_size: 32
    .language:       OpenCL C
    .language_version:
      - 2
      - 0
    .max_flat_workgroup_size: 512
    .name:           _Z10attn64_fwdPKDF16_S0_S0_PDF16_
    .private_segment_fixed_size: 0
    .sgpr_count:     58
    .sgpr_spill_count: 0
    .symbol:         _Z10attn64_fwdPKDF16_S0_S0_PDF16_.kd
    .uniform_work_group_size: 1
    .uses_dynamic_stack: false
    .vgpr_count:     256
    .vgpr_spill_count: 0
    .wavefront_size: 64
  - .agpr_count:     0
    .args:
      - .address_space:  global
        .offset:         0
        .size:           8
        .value_kind:     global_buffer
      - .address_space:  global
        .offset:         8
        .size:           8
        .value_kind:     global_buffer
      - .address_space:  global
        .offset:         16
        .size:           8
        .value_kind:     global_buffer
      - .address_space:  global
        .offset:         24
        .size:           8
        .value_kind:     global_buffer
      - .address_space:  global
        .offset:         32
        .size:           8
        .value_kind:     global_buffer
      - .address_space:  global
        .offset:         40
        .size:           8
        .value_kind:     global_buffer
      - .actual_access:  read_only
        .address_space:  global
        .offset:         48
        .size:           8
        .value_kind:     global_buffer
      - .offset:         56
        .size:           4
        .value_kind:     by_value
      - .offset:         60
        .size:           4
        .value_kind:     by_value
      - .offset:         64
        .size:           4
        .value_kind:     by_value
    .group_segment_fixed_size: 32768
    .kernarg_segment_align: 8
    .kernarg_segment_size: 68
    .language:       OpenCL C
    .language_version:
      - 2
      - 0
    .max_flat_workgroup_size: 768
    .name:           _Z7gemm_dbILi256ELi192ELi64ELi96ELi64ELi2ELi1ELi4EEvPKDF16_S1_PfPDF16_S3_S3_PK15HIP_vector_typeIfLj2EEiii
    .private_segment_fixed_size: 0
    .sgpr_count:     27
    .sgpr_spill_count: 0
    .symbol:         _Z7gemm_dbILi256ELi192ELi64ELi96ELi64ELi2ELi1ELi4EEvPKDF16_S1_PfPDF16_S3_S3_PK15HIP_vector_typeIfLj2EEiii.kd
    .uniform_work_group_size: 1
    .uses_dynamic_stack: false
    .vgpr_count:     141
    .vgpr_spill_count: 0
    .wavefront_size: 64
  - .agpr_count:     0
    .args:
      - .address_space:  global
        .offset:         0
        .size:           8
        .value_kind:     global_buffer
      - .address_space:  global
        .offset:         8
        .size:           8
        .value_kind:     global_buffer
      - .address_space:  global
        .offset:         16
        .size:           8
        .value_kind:     global_buffer
      - .address_space:  global
        .offset:         24
        .size:           8
        .value_kind:     global_buffer
      - .address_space:  global
        .offset:         32
        .size:           8
        .value_kind:     global_buffer
      - .address_space:  global
        .offset:         40
        .size:           8
        .value_kind:     global_buffer
      - .actual_access:  read_only
        .address_space:  global
        .offset:         48
        .size:           8
        .value_kind:     global_buffer
      - .offset:         56
        .size:           4
        .value_kind:     by_value
      - .offset:         60
        .size:           4
        .value_kind:     by_value
      - .offset:         64
        .size:           4
        .value_kind:     by_value
    .group_segment_fixed_size: 0
    .kernarg_segment_align: 8
    .kernarg_segment_size: 68
    .language:       OpenCL C
    .language_version:
      - 2
      - 0
    .max_flat_workgroup_size: 512
    .name:           _Z7gemm_dbILi128ELi128ELi64ELi64ELi64ELi3ELi0ELi4EEvPKDF16_S1_PfPDF16_S3_S3_PK15HIP_vector_typeIfLj2EEiii
    .private_segment_fixed_size: 0
    .sgpr_count:     26
    .sgpr_spill_count: 0
    .symbol:         _Z7gemm_dbILi128ELi128ELi64ELi64ELi64ELi3ELi0ELi4EEvPKDF16_S1_PfPDF16_S3_S3_PK15HIP_vector_typeIfLj2EEiii.kd
    .uniform_work_group_size: 1
    .uses_dynamic_stack: false
    .vgpr_count:     168
    .vgpr_spill_count: 0
    .wavefront_size: 64
